# rope epilogue: second-half cos/sin table loads issued with the first half's (borrowed constant VGPRs restored), no store drain; out-proj fp8 residual loads hoisted likewise
# baseline (speedup 1.0000x reference)
; #define PG8_ST8(rs, b0, p, v) __builtin_amdgcn_raw_buffer_store_b64(v, rs, (int)((const char*)(p) - (const char*)(b0)), 0, 16)
; __device__ __forceinline__ unsigned cvt_pk_bf16(float lo, float hi) { unsigned r; asm volatile("v_cvt_pk_bf16_f32 %0, %1, %2" : "=v"(r) : "v"(lo), "v"(hi)); return r; }
;     __device__ __forceinline__ void operator()(const f32x4 (&acc)[2][2][4][2], const Unit& u, int wr, int wc, int fr, int fq) const {
;     ...
;             const float sc = (pn <= 6 || (pn >= 9 && pn <= 11)) ? qscale : 1.0f;
;             const int f = 16 * (wc & 1) + 4 * fq, col0 = pn * BM + 64 * (wc >> 1) + f;
; #pragma unroll
;             for (int ai = 0; ai < 2; ++ai) {
;                 f32x4 c4[4], s4[4];
; #pragma unroll
;                 for (int m = 0; m < 4; ++m) { const int row = row0 + ai * HALF + m * 16; c4[m] = *(const f32x4*)(rc + (size_t)row * 32 + f); s4[m] = *(const f32x4*)(rs + (size_t)row * 32 + f); }
;                 asm volatile("" ::: "memory");
; #pragma unroll
;                 for (int m = 0; m < 4; ++m) { const int row = row0 + ai * HALF + m * 16;
;                     const f32x4 cc = c4[m] * sc, ss = s4[m] * sc;
;                     bf16_t* rowp = P + (size_t)row * ldp + col0;
; #pragma unroll
;                     for (int bj = 0; bj < 2; ++bj) { const f32x4 x1 = acc[ai][bj][m][0], x2 = acc[ai][bj][m][1]; const f32x4 o1 = x1 * cc - x2 * ss, o2 = x2 * cc + x1 * ss;
;                         u32x2 w1, w2; w1.x = cvt_pk_bf16(o1[0], o1[1]); w1.y = cvt_pk_bf16(o1[2], o1[3]); w2.x = cvt_pk_bf16(o2[0], o2[1]); w2.y = cvt_pk_bf16(o2[2], o2[3]);
;                         PG8_ST8(rsp_, P, rowp + bj * HALF, w1); PG8_ST8(rsp_, P, rowp + bj * HALF + 32, w2); } }
.LBB0_230:
	v_lshl_add_u32 v164, s27, 8, v175
	s_add_i32 s27, s62, s56
	s_cmp_gt_i32 s27, 3
	s_mov_b64 s[34:35], -1
	s_cbranch_scc0 .LBB0_237
	s_cmp_lg_u32 s27, 8
	s_cselect_b64 s[34:35], -1, 0
	s_cmp_lt_u32 s27, 15
	s_cselect_b64 s[36:37], -1, 0
	s_and_b64 s[36:37], s[34:35], s[36:37]
	s_mov_b64 s[34:35], -1
	s_and_b64 vcc, exec, s[36:37]
	v_add_u32_e32 v172, 0x80, v164
	v_add_u32_e32 v170, 0x90, v164
	v_add_u32_e32 v168, 0xa0, v164
	v_add_u32_e32 v166, 0xb0, v164
	s_cbranch_vccz .LBB0_233
	s_cmp_lt_u32 s27, 7
	s_cselect_b64 s[34:35], -1, 0
	s_add_i32 s36, s27, -9
	s_cmp_lt_u32 s36, 3
	s_cselect_b64 s[36:37], -1, 0
	s_or_b64 vcc, s[34:35], s[36:37]
	v_mov_b32_e32 v132, 0x3e38aa3b
	v_ashrrev_i32_e32 v165, 31, v164
	v_cndmask_b32_e32 v174, 1.0, v132, vcc
	s_mov_b32 vcc_lo, 0x4000
	s_mov_b32 vcc_hi, 0
	v_lshlrev_b64 v[132:133], 7, v[164:165]
	v_lshl_add_u64 v[134:135], v[154:155], 0, v[132:133]
	v_lshl_add_u64 v[132:133], v[156:157], 0, v[132:133]
	v_lshl_add_u64 v[228:229], v[134:135], 0, vcc
	global_load_dwordx4 v[176:179], v[134:135], off
	global_load_dwordx4 v[228:231], v[228:229], off
	v_lshl_add_u64 v[232:233], v[132:133], 0, vcc
	global_load_dwordx4 v[184:187], v[132:133], off
	global_load_dwordx4 v[232:235], v[232:233], off
	v_or_b32_e32 v192, 16, v164
	v_ashrrev_i32_e32 v193, 31, v192
	v_lshlrev_b64 v[132:133], 7, v[192:193]
	v_lshl_add_u64 v[134:135], v[154:155], 0, v[132:133]
	v_lshl_add_u64 v[132:133], v[156:157], 0, v[132:133]
	v_lshl_add_u64 v[236:237], v[134:135], 0, vcc
	global_load_dwordx4 v[188:191], v[134:135], off
	global_load_dwordx4 v[236:239], v[236:237], off
	v_lshl_add_u64 v[240:241], v[132:133], 0, vcc
	global_load_dwordx4 v[218:221], v[132:133], off
	global_load_dwordx4 v[240:243], v[240:241], off
	v_or_b32_e32 v182, 32, v164
	v_ashrrev_i32_e32 v183, 31, v182
	v_lshlrev_b64 v[132:133], 7, v[182:183]
	v_lshl_add_u64 v[134:135], v[154:155], 0, v[132:133]
	v_lshl_add_u64 v[132:133], v[156:157], 0, v[132:133]
	v_lshl_add_u64 v[244:245], v[134:135], 0, vcc
	global_load_dwordx4 v[144:147], v[134:135], off
	global_load_dwordx4 v[244:247], v[244:245], off
	v_lshl_add_u64 v[248:249], v[132:133], 0, vcc
	global_load_dwordx4 v[140:143], v[132:133], off
	global_load_dwordx4 v[248:251], v[248:249], off
	v_or_b32_e32 v180, 48, v164
	v_ashrrev_i32_e32 v181, 31, v180
	v_lshlrev_b64 v[132:133], 7, v[180:181]
	v_lshl_add_u64 v[134:135], v[154:155], 0, v[132:133]
	v_lshl_add_u64 v[132:133], v[156:157], 0, v[132:133]
	v_lshl_add_u64 v[210:211], v[134:135], 0, vcc
	global_load_dwordx4 v[136:139], v[134:135], off
	global_load_dwordx4 v[210:213], v[210:211], off
	s_movk_i32 s36, 0x2400
	v_lshl_add_u64 v[214:215], v[132:133], 0, vcc
	global_load_dwordx4 v[132:135], v[132:133], off
	global_load_dwordx4 v[214:217], v[214:215], off
	v_ashrrev_i32_e32 v173, 31, v172
	v_ashrrev_i32_e32 v171, 31, v170
	v_ashrrev_i32_e32 v169, 31, v168
	v_ashrrev_i32_e32 v167, 31, v166
	s_waitcnt vmcnt(0)
	v_pk_mul_f32 v[198:199], v[174:175], v[178:179] op_sel_hi:[0,1]
	v_pk_mul_f32 v[186:187], v[174:175], v[186:187] op_sel_hi:[0,1]
	v_pk_mul_f32 v[184:185], v[174:175], v[184:185] op_sel_hi:[0,1]
	v_pk_mul_f32 v[200:201], v[174:175], v[176:177] op_sel_hi:[0,1]
	v_mov_b64_e32 v[176:177], s[20:21]
	v_pk_mul_f32 v[208:209], v[118:119], v[186:187]
	v_pk_mul_f32 v[222:223], v[116:117], v[184:185]
	v_mad_i64_i32 v[204:205], s[34:35], v164, s36, v[176:177]
	v_lshl_or_b32 v178, s27, 9, v202
	v_mov_b32_e32 v179, v2
	v_pk_fma_f32 v[208:209], v[126:127], v[198:199], v[208:209] neg_lo:[0,0,1] neg_hi:[0,0,1]
	v_pk_fma_f32 v[222:223], v[124:125], v[200:201], v[222:223] neg_lo:[0,0,1] neg_hi:[0,0,1]
	v_pk_mul_f32 v[224:225], v[126:127], v[186:187]
	v_pk_mul_f32 v[226:227], v[124:125], v[184:185]
	v_lshl_add_u64 v[204:205], v[204:205], 0, v[178:179]
	v_pk_fma_f32 v[224:225], v[118:119], v[198:199], v[224:225]
	v_pk_fma_f32 v[226:227], v[116:117], v[200:201], v[226:227]
	v_cvt_pk_bf16_f32 v222, v222, v223
	v_cvt_pk_bf16_f32 v223, v208, v209
	v_mad_i64_i32 v[192:193], s[34:35], v192, s36, v[176:177]
	v_cvt_pk_bf16_f32 v208, v226, v227
	v_cvt_pk_bf16_f32 v209, v224, v225
	global_store_dwordx2 v[204:205], v[222:223], off
	global_store_dwordx2 v[204:205], v[208:209], off offset:64
	v_pk_mul_f32 v[208:209], v[122:123], v[186:187]
	v_pk_mul_f32 v[222:223], v[120:121], v[184:185]
	v_pk_mul_f32 v[186:187], v[130:131], v[186:187]
	v_pk_mul_f32 v[184:185], v[128:129], v[184:185]
	v_pk_fma_f32 v[186:187], v[122:123], v[198:199], v[186:187]
	v_pk_fma_f32 v[184:185], v[120:121], v[200:201], v[184:185]
	v_pk_fma_f32 v[208:209], v[130:131], v[198:199], v[208:209] neg_lo:[0,0,1] neg_hi:[0,0,1]
	v_pk_fma_f32 v[222:223], v[128:129], v[200:201], v[222:223] neg_lo:[0,0,1] neg_hi:[0,0,1]
	v_lshl_add_u64 v[192:193], v[192:193], 0, v[178:179]
	v_cvt_pk_bf16_f32 v198, v222, v223
	v_cvt_pk_bf16_f32 v199, v208, v209
	v_cvt_pk_bf16_f32 v184, v184, v185
	v_cvt_pk_bf16_f32 v185, v186, v187
	v_pk_mul_f32 v[186:187], v[174:175], v[190:191] op_sel_hi:[0,1]
	v_pk_mul_f32 v[190:191], v[174:175], v[218:219] op_sel_hi:[0,1]
	global_store_dwordx2 v[204:205], v[198:199], off offset:256
	global_store_dwordx2 v[204:205], v[184:185], off offset:320
	v_pk_mul_f32 v[184:185], v[174:175], v[188:189] op_sel_hi:[0,1]
	v_pk_mul_f32 v[188:189], v[174:175], v[220:221] op_sel_hi:[0,1]
	v_pk_mul_f32 v[198:199], v[100:101], v[190:191]
	v_pk_mul_f32 v[200:201], v[102:103], v[188:189]
	v_pk_fma_f32 v[198:199], v[108:109], v[184:185], v[198:199] neg_lo:[0,0,1] neg_hi:[0,0,1]
	v_pk_fma_f32 v[200:201], v[110:111], v[186:187], v[200:201] neg_lo:[0,0,1] neg_hi:[0,0,1]
	v_pk_mul_f32 v[204:205], v[108:109], v[190:191]
; #define PG8_ST8(rs, b0, p, v) __builtin_amdgcn_raw_buffer_store_b64(v, rs, (int)((const char*)(p) - (const char*)(b0)), 0, 16)
; __device__ __forceinline__ unsigned cvt_pk_bf16(float lo, float hi) { unsigned r; asm volatile("v_cvt_pk_bf16_f32 %0, %1, %2" : "=v"(r) : "v"(lo), "v"(hi)); return r; }
;     __device__ __forceinline__ void operator()(const f32x4 (&acc)[2][2][4][2], const Unit& u, int wr, int wc, int fr, int fq) const {
;     ...
;                 for (int m = 0; m < 4; ++m) { const int row = row0 + ai * HALF + m * 16; c4[m] = *(const f32x4*)(rc + (size_t)row * 32 + f); s4[m] = *(const f32x4*)(rs + (size_t)row * 32 + f); }
;                 asm volatile("" ::: "memory");
; #pragma unroll
;                 for (int m = 0; m < 4; ++m) { const int row = row0 + ai * HALF + m * 16;
;                     const f32x4 cc = c4[m] * sc, ss = s4[m] * sc;
;                     bf16_t* rowp = P + (size_t)row * ldp + col0;
; #pragma unroll
;                     for (int bj = 0; bj < 2; ++bj) { const f32x4 x1 = acc[ai][bj][m][0], x2 = acc[ai][bj][m][1]; const f32x4 o1 = x1 * cc - x2 * ss, o2 = x2 * cc + x1 * ss;
;                         u32x2 w1, w2; w1.x = cvt_pk_bf16(o1[0], o1[1]); w1.y = cvt_pk_bf16(o1[2], o1[3]); w2.x = cvt_pk_bf16(o2[0], o2[1]); w2.y = cvt_pk_bf16(o2[2], o2[3]);
;                         PG8_ST8(rsp_, P, rowp + bj * HALF, w1); PG8_ST8(rsp_, P, rowp + bj * HALF + 32, w2); } }
	v_pk_mul_f32 v[208:209], v[110:111], v[188:189]
	v_cvt_pk_bf16_f32 v198, v198, v199
	v_cvt_pk_bf16_f32 v199, v200, v201
	v_pk_fma_f32 v[204:205], v[100:101], v[184:185], v[204:205]
	v_pk_fma_f32 v[208:209], v[102:103], v[186:187], v[208:209]
	v_cvt_pk_bf16_f32 v200, v204, v205
	v_pk_mul_f32 v[142:143], v[174:175], v[142:143] op_sel_hi:[0,1]
	v_cvt_pk_bf16_f32 v201, v208, v209
	global_store_dwordx2 v[192:193], v[198:199], off
	global_store_dwordx2 v[192:193], v[200:201], off offset:64
	v_pk_mul_f32 v[198:199], v[104:105], v[190:191]
	v_pk_mul_f32 v[190:191], v[112:113], v[190:191]
	v_pk_mul_f32 v[200:201], v[106:107], v[188:189]
	v_pk_fma_f32 v[198:199], v[112:113], v[184:185], v[198:199] neg_lo:[0,0,1] neg_hi:[0,0,1]
	v_pk_mul_f32 v[188:189], v[114:115], v[188:189]
	v_pk_fma_f32 v[184:185], v[104:105], v[184:185], v[190:191]
	v_pk_fma_f32 v[200:201], v[114:115], v[186:187], v[200:201] neg_lo:[0,0,1] neg_hi:[0,0,1]
	v_pk_fma_f32 v[186:187], v[106:107], v[186:187], v[188:189]
	v_cvt_pk_bf16_f32 v188, v198, v199
	v_cvt_pk_bf16_f32 v189, v200, v201
	v_cvt_pk_bf16_f32 v184, v184, v185
	v_pk_mul_f32 v[140:141], v[174:175], v[140:141] op_sel_hi:[0,1]
	v_cvt_pk_bf16_f32 v185, v186, v187
	global_store_dwordx2 v[192:193], v[188:189], off offset:256
	global_store_dwordx2 v[192:193], v[184:185], off offset:320
	v_pk_mul_f32 v[144:145], v[174:175], v[144:145] op_sel_hi:[0,1]
	v_pk_mul_f32 v[146:147], v[174:175], v[146:147] op_sel_hi:[0,1]
	v_pk_mul_f32 v[184:185], v[84:85], v[140:141]
	v_pk_mul_f32 v[186:187], v[86:87], v[142:143]
	v_mad_i64_i32 v[182:183], s[34:35], v182, s36, v[176:177]
	v_pk_fma_f32 v[186:187], v[94:95], v[146:147], v[186:187] neg_lo:[0,0,1] neg_hi:[0,0,1]
	v_pk_fma_f32 v[184:185], v[92:93], v[144:145], v[184:185] neg_lo:[0,0,1] neg_hi:[0,0,1]
	v_pk_mul_f32 v[188:189], v[92:93], v[140:141]
	v_pk_mul_f32 v[190:191], v[94:95], v[142:143]
	v_lshl_add_u64 v[182:183], v[182:183], 0, v[178:179]
	v_pk_fma_f32 v[190:191], v[86:87], v[146:147], v[190:191]
	v_pk_fma_f32 v[188:189], v[84:85], v[144:145], v[188:189]
	v_cvt_pk_bf16_f32 v184, v184, v185
	v_cvt_pk_bf16_f32 v185, v186, v187
	v_pk_mul_f32 v[134:135], v[174:175], v[134:135] op_sel_hi:[0,1]
	v_cvt_pk_bf16_f32 v186, v188, v189
	v_cvt_pk_bf16_f32 v187, v190, v191
	global_store_dwordx2 v[182:183], v[184:185], off
	global_store_dwordx2 v[182:183], v[186:187], off offset:64
	v_pk_mul_f32 v[184:185], v[88:89], v[140:141]
	v_pk_mul_f32 v[186:187], v[90:91], v[142:143]
	v_pk_mul_f32 v[140:141], v[96:97], v[140:141]
	v_pk_mul_f32 v[142:143], v[98:99], v[142:143]
	v_pk_fma_f32 v[186:187], v[98:99], v[146:147], v[186:187] neg_lo:[0,0,1] neg_hi:[0,0,1]
	v_pk_fma_f32 v[184:185], v[96:97], v[144:145], v[184:185] neg_lo:[0,0,1] neg_hi:[0,0,1]
	v_pk_fma_f32 v[142:143], v[90:91], v[146:147], v[142:143]
	v_pk_fma_f32 v[140:141], v[88:89], v[144:145], v[140:141]
	v_cvt_pk_bf16_f32 v144, v184, v185
	v_cvt_pk_bf16_f32 v145, v186, v187
	v_pk_mul_f32 v[132:133], v[174:175], v[132:133] op_sel_hi:[0,1]
	v_cvt_pk_bf16_f32 v140, v140, v141
	v_cvt_pk_bf16_f32 v141, v142, v143
	global_store_dwordx2 v[182:183], v[144:145], off offset:256
	global_store_dwordx2 v[182:183], v[140:141], off offset:320
	v_pk_mul_f32 v[136:137], v[174:175], v[136:137] op_sel_hi:[0,1]
	v_pk_mul_f32 v[138:139], v[174:175], v[138:139] op_sel_hi:[0,1]
	v_pk_mul_f32 v[142:143], v[68:69], v[132:133]
	v_pk_mul_f32 v[144:145], v[70:71], v[134:135]
	v_mad_i64_i32 v[140:141], s[34:35], v180, s36, v[176:177]
	v_pk_fma_f32 v[144:145], v[78:79], v[138:139], v[144:145] neg_lo:[0,0,1] neg_hi:[0,0,1]
	v_pk_fma_f32 v[142:143], v[76:77], v[136:137], v[142:143] neg_lo:[0,0,1] neg_hi:[0,0,1]
	v_pk_mul_f32 v[146:147], v[76:77], v[132:133]
	v_pk_mul_f32 v[180:181], v[78:79], v[134:135]
	v_lshl_add_u64 v[140:141], v[140:141], 0, v[178:179]
	v_pk_fma_f32 v[180:181], v[70:71], v[138:139], v[180:181]
	v_pk_fma_f32 v[146:147], v[68:69], v[136:137], v[146:147]
	v_cvt_pk_bf16_f32 v142, v142, v143
	v_cvt_pk_bf16_f32 v143, v144, v145
	v_lshlrev_b64 v[184:185], 7, v[168:169]
	v_cvt_pk_bf16_f32 v144, v146, v147
	v_cvt_pk_bf16_f32 v145, v180, v181
	global_store_dwordx2 v[140:141], v[142:143], off
	global_store_dwordx2 v[140:141], v[144:145], off offset:64
	v_pk_mul_f32 v[142:143], v[72:73], v[132:133]
	v_pk_mul_f32 v[144:145], v[74:75], v[134:135]
	v_pk_mul_f32 v[132:133], v[80:81], v[132:133]
	v_pk_fma_f32 v[144:145], v[82:83], v[138:139], v[144:145] neg_lo:[0,0,1] neg_hi:[0,0,1]
	v_pk_fma_f32 v[142:143], v[80:81], v[136:137], v[142:143] neg_lo:[0,0,1] neg_hi:[0,0,1]
	v_pk_mul_f32 v[134:135], v[82:83], v[134:135]
	v_pk_fma_f32 v[132:133], v[72:73], v[136:137], v[132:133]
	v_cvt_pk_bf16_f32 v136, v142, v143
	v_cvt_pk_bf16_f32 v137, v144, v145
	v_pk_fma_f32 v[134:135], v[74:75], v[138:139], v[134:135]
	v_cvt_pk_bf16_f32 v132, v132, v133
	v_lshlrev_b64 v[144:145], 7, v[170:171]
	v_cvt_pk_bf16_f32 v133, v134, v135
	global_store_dwordx2 v[140:141], v[136:137], off offset:256
	global_store_dwordx2 v[140:141], v[132:133], off offset:320
	v_lshlrev_b64 v[136:137], 7, v[172:173]
	v_lshl_add_u64 v[132:133], v[154:155], 0, v[136:137]
	v_lshl_add_u64 v[136:137], v[156:157], 0, v[136:137]
	v_lshl_add_u64 v[140:141], v[154:155], 0, v[144:145]
	v_lshl_add_u64 v[144:145], v[156:157], 0, v[144:145]
	v_lshl_add_u64 v[180:181], v[154:155], 0, v[184:185]
	v_lshl_add_u64 v[184:185], v[156:157], 0, v[184:185]
	v_lshlrev_b64 v[192:193], 7, v[166:167]
	v_lshl_add_u64 v[188:189], v[154:155], 0, v[192:193]
	v_lshl_add_u64 v[192:193], v[156:157], 0, v[192:193]
	s_waitcnt vmcnt(16)
; #define PG8_ST8(rs, b0, p, v) __builtin_amdgcn_raw_buffer_store_b64(v, rs, (int)((const char*)(p) - (const char*)(b0)), 0, 16)
; __device__ __forceinline__ unsigned cvt_pk_bf16(float lo, float hi) { unsigned r; asm volatile("v_cvt_pk_bf16_f32 %0, %1, %2" : "=v"(r) : "v"(lo), "v"(hi)); return r; }
;     __device__ __forceinline__ void operator()(const f32x4 (&acc)[2][2][4][2], const Unit& u, int wr, int wc, int fr, int fq) const {
;     ...
;                 for (int m = 0; m < 4; ++m) { const int row = row0 + ai * HALF + m * 16;
;                     const f32x4 cc = c4[m] * sc, ss = s4[m] * sc;
;                     bf16_t* rowp = P + (size_t)row * ldp + col0;
; #pragma unroll
;                     for (int bj = 0; bj < 2; ++bj) { const f32x4 x1 = acc[ai][bj][m][0], x2 = acc[ai][bj][m][1]; const f32x4 o1 = x1 * cc - x2 * ss, o2 = x2 * cc + x1 * ss;
;                         u32x2 w1, w2; w1.x = cvt_pk_bf16(o1[0], o1[1]); w1.y = cvt_pk_bf16(o1[2], o1[3]); w2.x = cvt_pk_bf16(o2[0], o2[1]); w2.y = cvt_pk_bf16(o2[2], o2[3]);
;                         PG8_ST8(rsp_, P, rowp + bj * HALF, w1); PG8_ST8(rsp_, P, rowp + bj * HALF + 32, w2); } }
	v_mov_b32_e32 v132, v228
	v_mov_b32_e32 v133, v229
	v_mov_b32_e32 v134, v230
	v_mov_b32_e32 v135, v231
	v_mov_b32_e32 v136, v232
	v_mov_b32_e32 v137, v233
	v_mov_b32_e32 v138, v234
	v_mov_b32_e32 v139, v235
	v_mov_b32_e32 v140, v236
	v_mov_b32_e32 v141, v237
	v_mov_b32_e32 v142, v238
	v_mov_b32_e32 v143, v239
	v_mov_b32_e32 v144, v240
	v_mov_b32_e32 v145, v241
	v_mov_b32_e32 v146, v242
	v_mov_b32_e32 v147, v243
	v_mov_b32_e32 v180, v244
	v_mov_b32_e32 v181, v245
	v_mov_b32_e32 v182, v246
	v_mov_b32_e32 v183, v247
	v_mov_b32_e32 v184, v248
	v_mov_b32_e32 v185, v249
	v_mov_b32_e32 v186, v250
	v_mov_b32_e32 v187, v251
	v_mov_b32_e32 v188, v210
	v_mov_b32_e32 v189, v211
	v_mov_b32_e32 v190, v212
	v_mov_b32_e32 v191, v213
	v_mov_b32_e32 v218, v214
	v_mov_b32_e32 v219, v215
	v_mov_b32_e32 v220, v216
	v_mov_b32_e32 v221, v217
	v_pk_mul_f32 v[132:133], v[174:175], v[132:133] op_sel_hi:[0,1]
	v_pk_mul_f32 v[138:139], v[174:175], v[138:139] op_sel_hi:[0,1]
	v_pk_mul_f32 v[136:137], v[174:175], v[136:137] op_sel_hi:[0,1]
	v_pk_mul_f32 v[134:135], v[174:175], v[134:135] op_sel_hi:[0,1]
	v_pk_mul_f32 v[198:199], v[52:53], v[136:137]
	v_pk_mul_f32 v[200:201], v[54:55], v[138:139]
	v_mad_i64_i32 v[192:193], s[34:35], v172, s36, v[176:177]
	v_pk_fma_f32 v[200:201], v[62:63], v[134:135], v[200:201] neg_lo:[0,0,1] neg_hi:[0,0,1]
	v_pk_fma_f32 v[198:199], v[60:61], v[132:133], v[198:199] neg_lo:[0,0,1] neg_hi:[0,0,1]
	v_pk_mul_f32 v[204:205], v[60:61], v[136:137]
	v_pk_mul_f32 v[208:209], v[62:63], v[138:139]
	v_lshl_add_u64 v[192:193], v[192:193], 0, v[178:179]
	v_pk_fma_f32 v[208:209], v[54:55], v[134:135], v[208:209]
	v_pk_fma_f32 v[204:205], v[52:53], v[132:133], v[204:205]
	v_cvt_pk_bf16_f32 v198, v198, v199
	v_cvt_pk_bf16_f32 v199, v200, v201
	s_nop 0
	v_cvt_pk_bf16_f32 v200, v204, v205
	v_cvt_pk_bf16_f32 v201, v208, v209
	global_store_dwordx2 v[192:193], v[198:199], off
	global_store_dwordx2 v[192:193], v[200:201], off offset:64
	v_pk_mul_f32 v[198:199], v[56:57], v[136:137]
	v_pk_mul_f32 v[200:201], v[58:59], v[138:139]
	v_pk_mul_f32 v[136:137], v[64:65], v[136:137]
	v_pk_fma_f32 v[200:201], v[66:67], v[134:135], v[200:201] neg_lo:[0,0,1] neg_hi:[0,0,1]
	v_pk_fma_f32 v[198:199], v[64:65], v[132:133], v[198:199] neg_lo:[0,0,1] neg_hi:[0,0,1]
	v_pk_mul_f32 v[138:139], v[66:67], v[138:139]
	v_pk_fma_f32 v[132:133], v[56:57], v[132:133], v[136:137]
	v_cvt_pk_bf16_f32 v136, v198, v199
	v_cvt_pk_bf16_f32 v137, v200, v201
	v_pk_fma_f32 v[134:135], v[58:59], v[134:135], v[138:139]
	v_cvt_pk_bf16_f32 v132, v132, v133
	v_pk_mul_f32 v[138:139], v[174:175], v[144:145] op_sel_hi:[0,1]
	v_cvt_pk_bf16_f32 v133, v134, v135
	global_store_dwordx2 v[192:193], v[136:137], off offset:256
	global_store_dwordx2 v[192:193], v[132:133], off offset:320
	v_pk_mul_f32 v[136:137], v[174:175], v[146:147] op_sel_hi:[0,1]
	v_pk_mul_f32 v[132:133], v[174:175], v[140:141] op_sel_hi:[0,1]
	v_pk_mul_f32 v[134:135], v[174:175], v[142:143] op_sel_hi:[0,1]
	v_pk_mul_f32 v[142:143], v[36:37], v[138:139]
	v_pk_mul_f32 v[144:145], v[38:39], v[136:137]
	v_mad_i64_i32 v[140:141], s[34:35], v170, s36, v[176:177]
	v_pk_fma_f32 v[144:145], v[46:47], v[134:135], v[144:145] neg_lo:[0,0,1] neg_hi:[0,0,1]
	v_pk_fma_f32 v[142:143], v[44:45], v[132:133], v[142:143] neg_lo:[0,0,1] neg_hi:[0,0,1]
	v_pk_mul_f32 v[146:147], v[44:45], v[138:139]
	v_pk_mul_f32 v[192:193], v[46:47], v[136:137]
	v_lshl_add_u64 v[140:141], v[140:141], 0, v[178:179]
	v_pk_fma_f32 v[192:193], v[38:39], v[134:135], v[192:193]
	v_pk_fma_f32 v[146:147], v[36:37], v[132:133], v[146:147]
	v_cvt_pk_bf16_f32 v142, v142, v143
	v_cvt_pk_bf16_f32 v143, v144, v145
	s_nop 0
	v_cvt_pk_bf16_f32 v144, v146, v147
	v_cvt_pk_bf16_f32 v145, v192, v193
	global_store_dwordx2 v[140:141], v[142:143], off
	global_store_dwordx2 v[140:141], v[144:145], off offset:64
	v_pk_mul_f32 v[142:143], v[40:41], v[138:139]
	v_pk_mul_f32 v[144:145], v[42:43], v[136:137]
	v_pk_mul_f32 v[138:139], v[48:49], v[138:139]
	v_pk_mul_f32 v[136:137], v[50:51], v[136:137]
	v_pk_fma_f32 v[144:145], v[50:51], v[134:135], v[144:145] neg_lo:[0,0,1] neg_hi:[0,0,1]
	v_pk_fma_f32 v[142:143], v[48:49], v[132:133], v[142:143] neg_lo:[0,0,1] neg_hi:[0,0,1]
	v_pk_fma_f32 v[134:135], v[42:43], v[134:135], v[136:137]
	v_pk_fma_f32 v[132:133], v[40:41], v[132:133], v[138:139]
; #define PG8_ST8(rs, b0, p, v) __builtin_amdgcn_raw_buffer_store_b64(v, rs, (int)((const char*)(p) - (const char*)(b0)), 0, 16)
; __device__ __forceinline__ unsigned cvt_pk_bf16(float lo, float hi) { unsigned r; asm volatile("v_cvt_pk_bf16_f32 %0, %1, %2" : "=v"(r) : "v"(lo), "v"(hi)); return r; }
;     __device__ __forceinline__ void operator()(const f32x4 (&acc)[2][2][4][2], const Unit& u, int wr, int wc, int fr, int fq) const {
;     ...
;                 for (int m = 0; m < 4; ++m) { const int row = row0 + ai * HALF + m * 16;
;                     const f32x4 cc = c4[m] * sc, ss = s4[m] * sc;
;                     bf16_t* rowp = P + (size_t)row * ldp + col0;
; #pragma unroll
;                     for (int bj = 0; bj < 2; ++bj) { const f32x4 x1 = acc[ai][bj][m][0], x2 = acc[ai][bj][m][1]; const f32x4 o1 = x1 * cc - x2 * ss, o2 = x2 * cc + x1 * ss;
;                         u32x2 w1, w2; w1.x = cvt_pk_bf16(o1[0], o1[1]); w1.y = cvt_pk_bf16(o1[2], o1[3]); w2.x = cvt_pk_bf16(o2[0], o2[1]); w2.y = cvt_pk_bf16(o2[2], o2[3]);
;                         PG8_ST8(rsp_, P, rowp + bj * HALF, w1); PG8_ST8(rsp_, P, rowp + bj * HALF + 32, w2); } }
	v_cvt_pk_bf16_f32 v136, v142, v143
	v_cvt_pk_bf16_f32 v137, v144, v145
	v_pk_mul_f32 v[138:139], v[174:175], v[184:185] op_sel_hi:[0,1]
	v_cvt_pk_bf16_f32 v132, v132, v133
	v_cvt_pk_bf16_f32 v133, v134, v135
	global_store_dwordx2 v[140:141], v[136:137], off offset:256
	global_store_dwordx2 v[140:141], v[132:133], off offset:320
	v_pk_mul_f32 v[136:137], v[174:175], v[186:187] op_sel_hi:[0,1]
	v_pk_mul_f32 v[132:133], v[174:175], v[180:181] op_sel_hi:[0,1]
	v_pk_mul_f32 v[134:135], v[174:175], v[182:183] op_sel_hi:[0,1]
	v_pk_mul_f32 v[142:143], v[20:21], v[138:139]
	v_pk_mul_f32 v[144:145], v[22:23], v[136:137]
	v_mad_i64_i32 v[140:141], s[34:35], v168, s36, v[176:177]
	v_pk_fma_f32 v[144:145], v[30:31], v[134:135], v[144:145] neg_lo:[0,0,1] neg_hi:[0,0,1]
	v_pk_fma_f32 v[142:143], v[28:29], v[132:133], v[142:143] neg_lo:[0,0,1] neg_hi:[0,0,1]
	v_pk_mul_f32 v[146:147], v[28:29], v[138:139]
	v_pk_mul_f32 v[180:181], v[30:31], v[136:137]
	v_lshl_add_u64 v[140:141], v[140:141], 0, v[178:179]
	v_pk_fma_f32 v[180:181], v[22:23], v[134:135], v[180:181]
	v_pk_fma_f32 v[146:147], v[20:21], v[132:133], v[146:147]
	v_cvt_pk_bf16_f32 v142, v142, v143
	v_cvt_pk_bf16_f32 v143, v144, v145
	s_nop 0
	v_cvt_pk_bf16_f32 v144, v146, v147
	v_cvt_pk_bf16_f32 v145, v180, v181
	global_store_dwordx2 v[140:141], v[142:143], off
	global_store_dwordx2 v[140:141], v[144:145], off offset:64
	v_pk_mul_f32 v[142:143], v[24:25], v[138:139]
	v_pk_mul_f32 v[144:145], v[26:27], v[136:137]
	v_pk_mul_f32 v[138:139], v[32:33], v[138:139]
	v_pk_mul_f32 v[136:137], v[34:35], v[136:137]
	v_pk_fma_f32 v[144:145], v[34:35], v[134:135], v[144:145] neg_lo:[0,0,1] neg_hi:[0,0,1]
	v_pk_fma_f32 v[142:143], v[32:33], v[132:133], v[142:143] neg_lo:[0,0,1] neg_hi:[0,0,1]
	v_pk_fma_f32 v[134:135], v[26:27], v[134:135], v[136:137]
	v_pk_fma_f32 v[132:133], v[24:25], v[132:133], v[138:139]
	v_cvt_pk_bf16_f32 v136, v142, v143
	v_cvt_pk_bf16_f32 v137, v144, v145
	v_pk_mul_f32 v[138:139], v[174:175], v[218:219] op_sel_hi:[0,1]
	v_cvt_pk_bf16_f32 v132, v132, v133
	v_cvt_pk_bf16_f32 v133, v134, v135
	global_store_dwordx2 v[140:141], v[136:137], off offset:256
	global_store_dwordx2 v[140:141], v[132:133], off offset:320
	v_pk_mul_f32 v[136:137], v[174:175], v[220:221] op_sel_hi:[0,1]
	v_pk_mul_f32 v[132:133], v[174:175], v[188:189] op_sel_hi:[0,1]
	v_pk_mul_f32 v[134:135], v[174:175], v[190:191] op_sel_hi:[0,1]
	v_pk_mul_f32 v[142:143], v[4:5], v[138:139]
	v_pk_mul_f32 v[144:145], v[6:7], v[136:137]
	v_mad_i64_i32 v[140:141], s[34:35], v166, s36, v[176:177]
	v_pk_fma_f32 v[144:145], v[14:15], v[134:135], v[144:145] neg_lo:[0,0,1] neg_hi:[0,0,1]
	v_pk_fma_f32 v[142:143], v[12:13], v[132:133], v[142:143] neg_lo:[0,0,1] neg_hi:[0,0,1]
	v_pk_mul_f32 v[146:147], v[12:13], v[138:139]
	v_pk_mul_f32 v[176:177], v[14:15], v[136:137]
	v_lshl_add_u64 v[140:141], v[140:141], 0, v[178:179]
	v_pk_fma_f32 v[176:177], v[6:7], v[134:135], v[176:177]
	v_pk_fma_f32 v[146:147], v[4:5], v[132:133], v[146:147]
	v_cvt_pk_bf16_f32 v142, v142, v143
	v_cvt_pk_bf16_f32 v143, v144, v145
	s_mov_b64 s[34:35], 0
	v_cvt_pk_bf16_f32 v144, v146, v147
	v_cvt_pk_bf16_f32 v145, v176, v177
	global_store_dwordx2 v[140:141], v[142:143], off
	global_store_dwordx2 v[140:141], v[144:145], off offset:64
	v_pk_mul_f32 v[142:143], v[8:9], v[138:139]
	v_pk_mul_f32 v[144:145], v[10:11], v[136:137]
	v_pk_mul_f32 v[138:139], v[16:17], v[138:139]
	v_pk_mul_f32 v[136:137], v[18:19], v[136:137]
	v_pk_fma_f32 v[144:145], v[18:19], v[134:135], v[144:145] neg_lo:[0,0,1] neg_hi:[0,0,1]
	v_pk_fma_f32 v[142:143], v[16:17], v[132:133], v[142:143] neg_lo:[0,0,1] neg_hi:[0,0,1]
	v_pk_fma_f32 v[134:135], v[10:11], v[134:135], v[136:137]
	v_pk_fma_f32 v[132:133], v[8:9], v[132:133], v[138:139]
	v_cvt_pk_bf16_f32 v136, v142, v143
	v_cvt_pk_bf16_f32 v137, v144, v145
	s_nop 0
	v_cvt_pk_bf16_f32 v132, v132, v133
	v_cvt_pk_bf16_f32 v133, v134, v135
	global_store_dwordx2 v[140:141], v[136:137], off offset:256
	global_store_dwordx2 v[140:141], v[132:133], off offset:320
	v_mov_b32_e32 v210, 0x3727c5ac
	v_mov_b32_e32 v211, 0x260
	v_mov_b32_e32 v212, 0x358637bd
	v_mov_b32_e32 v213, -1
	v_mov_b32_e32 v214, 0x43e00000
	v_mbcnt_lo_u32_b32 v215, -1, 0
	v_mbcnt_hi_u32_b32 v215, -1, v215
	v_mov_b32_e32 v216, 0xff800000
	v_mov_b64_e32 v[250:251], 0x200

; #define PG8_ST16(rs, b0, p, v) __builtin_amdgcn_raw_buffer_store_b128(v, rs, (int)((const char*)(p) - (const char*)(b0)), 0, 16)
; __device__ __forceinline__ unsigned cvt_pk_bf16(float lo, float hi) { unsigned r; asm volatile("v_cvt_pk_bf16_f32 %0, %1, %2" : "=v"(r) : "v"(lo), "v"(hi)); return r; }
;     __device__ __forceinline__ void operator()(const f32x4 (&acc)[2][2][4][2], const Unit& u, int wr, int wc, int fr, int fq) const {
;     ...
;             for (int m = 0; m < 4; ++m) { const size_t off = (size_t)(row0 + ai * HALF + m * 16) * ldc + col0;
; #pragma unroll
;                 for (int bj = 0; bj < 2; ++bj) {
;                     if (BASE_F32) { b0[m][bj] = *(const f32x4*)((const float*)base + off + bj * HALF); b1[m][bj] = *(const f32x4*)((const float*)base + off + bj * HALF + 4); }
;                     else { const u32x4 q = *(const u32x4*)((const bf16_t*)base + off + bj * HALF);
;                         b0[m][bj] = (f32x4){__uint_as_float(q.x << 16), __uint_as_float(q.x & 0xffff0000u), __uint_as_float(q.y << 16), __uint_as_float(q.y & 0xffff0000u)};
;                         b1[m][bj] = (f32x4){__uint_as_float(q.z << 16), __uint_as_float(q.z & 0xffff0000u), __uint_as_float(q.w << 16), __uint_as_float(q.w & 0xffff0000u)}; } } }
;             asm volatile("" ::: "memory");
; #pragma unroll
;             for (int m = 0; m < 4; ++m) { const size_t off = (size_t)(row0 + ai * HALF + m * 16) * ldc + col0; float ssq = 0.f;
; #pragma unroll
;                 for (int bj = 0; bj < 2; ++bj) {
;                     const f32x4 o0 = b0[m][bj] + acc[ai][bj][m][0] * sc, o1 = b1[m][bj] + acc[ai][bj][m][1] * sc;
;                     ssq += ((o0[0] * o0[0] + o0[1] * o0[1]) + (o0[2] * o0[2] + o0[3] * o0[3])) + ((o1[0] * o1[0] + o1[1] * o1[1]) + (o1[2] * o1[2] + o1[3] * o1[3]));
;                     u32x4 w; w.x = cvt_pk_bf16(o0[0], o0[1]); w.y = cvt_pk_bf16(o0[2], o0[3]); w.z = cvt_pk_bf16(o1[0], o1[1]); w.w = cvt_pk_bf16(o1[2], o1[3]);
;                     PG8_ST16(rs_, out, out + off + bj * HALF, w); }
;                 ssq += __shfl_xor(ssq, 16); ssq += __shfl_xor(ssq, 32);
;                 if (fq == 0) rowss[(size_t)(row0 + ai * HALF + m * 16) * 32 + 4 * u.pn + wc] = ssq; }
.LBB0_822:
	v_lshl_or_b32 v36, s70, 8, v188
	v_lshl_add_u32 v38, s71, 8, v186
	v_ashrrev_i32_e32 v37, 31, v36
	v_lshlrev_b64 v[192:193], 1, v[36:37]
	v_ashrrev_i32_e32 v39, 31, v38
	v_lshl_add_u64 v[40:41], s[20:21], 0, v[192:193]
	v_lshlrev_b64 v[190:191], 12, v[38:39]
	v_lshl_add_u64 v[4:5], v[40:41], 0, v[190:191]
	global_load_dwordx4 v[60:63], v[4:5], off
	global_load_dwordx4 v[76:79], v[4:5], off offset:256
	s_mov_b32 s46, 0x80000
	s_mov_b32 s47, 0
	v_lshl_add_u64 v[248:249], v[4:5], 0, s[46:47]
	v_or_b32_e32 v54, 16, v38
	v_or_b32_e32 v52, 32, v38
	v_or_b32_e32 v42, 48, v38
	v_ashrrev_i32_e32 v55, 31, v54
	v_ashrrev_i32_e32 v53, 31, v52
	v_ashrrev_i32_e32 v43, 31, v42
	v_lshlrev_b64 v[4:5], 12, v[54:55]
	v_lshlrev_b64 v[6:7], 12, v[52:53]
	v_lshlrev_b64 v[8:9], 12, v[42:43]
	v_lshl_add_u64 v[4:5], v[40:41], 0, v[4:5]
	v_lshl_add_u64 v[6:7], v[40:41], 0, v[6:7]
	v_lshl_add_u64 v[194:195], v[40:41], 0, v[8:9]
	v_lshl_add_u64 v[246:247], v[4:5], 0, s[46:47]
	v_lshl_add_u64 v[244:245], v[6:7], 0, s[46:47]
	v_lshl_add_u64 v[242:243], v[194:195], 0, s[46:47]
	global_load_dwordx4 v[24:27], v[4:5], off
	global_load_dwordx4 v[20:23], v[4:5], off offset:256
	global_load_dwordx4 v[16:19], v[6:7], off
	global_load_dwordx4 v[12:15], v[6:7], off offset:256
	global_load_dwordx4 v[8:11], v[194:195], off
	s_nop 0
	global_load_dwordx4 v[4:7], v[194:195], off offset:256
	global_load_dwordx4 v[222:225], v[248:249], off
	global_load_dwordx4 v[218:221], v[248:249], off offset:256
	global_load_dwordx4 v[226:229], v[246:247], off
	global_load_dwordx4 v[230:233], v[246:247], off offset:256
	global_load_dwordx4 v[234:237], v[244:245], off
	global_load_dwordx4 v[238:241], v[244:245], off offset:256
	v_mov_b32_e32 v248, v242
	v_mov_b32_e32 v249, v243
	global_load_dwordx4 v[246:249], v[248:249], off offset:256
	global_load_dwordx4 v[242:245], v[242:243], off
	v_and_b32_e32 v195, 64, v215
	v_xor_b32_e32 v194, 16, v215
	v_add_u32_e32 v195, 64, v195
	v_xor_b32_e32 v196, 32, v215
	v_cmp_lt_i32_e32 vcc, v194, v195
	s_lshl_b32 s42, s70, 2
	s_ashr_i32 s43, s42, 31
	v_cndmask_b32_e32 v197, v215, v194, vcc
	v_cmp_lt_i32_e32 vcc, v196, v195
	v_lshl_add_u64 v[194:195], s[20:21], 0, v[190:191]
	v_lshlrev_b32_e32 v190, 2, v197
	v_cndmask_b32_e32 v202, v215, v196, vcc
	v_lshl_add_u64 v[192:193], v[194:195], 0, v[192:193]
	s_waitcnt vmcnt(8)
	v_lshlrev_b32_e32 v194, 16, v60
	v_and_b32_e32 v195, 0xffff0000, v60
	v_lshlrev_b32_e32 v60, 16, v61
	v_and_b32_e32 v61, 0xffff0000, v61
	v_lshlrev_b32_e32 v196, 16, v62
	v_and_b32_e32 v197, 0xffff0000, v62
	v_lshlrev_b32_e32 v62, 16, v63
	v_and_b32_e32 v63, 0xffff0000, v63
	v_lshlrev_b32_e32 v198, 16, v76
	v_and_b32_e32 v199, 0xffff0000, v76
	v_lshlrev_b32_e32 v76, 16, v77
	v_and_b32_e32 v77, 0xffff0000, v77
	v_lshlrev_b32_e32 v200, 16, v78
	v_and_b32_e32 v201, 0xffff0000, v78
	v_lshlrev_b32_e32 v78, 16, v79
	v_and_b32_e32 v79, 0xffff0000, v79
	v_pk_add_f32 v[162:163], v[162:163], v[60:61]
	v_pk_add_f32 v[160:161], v[160:161], v[194:195]
	v_pk_add_f32 v[174:175], v[174:175], v[62:63]
	v_pk_add_f32 v[62:63], v[176:177], v[196:197]
	v_pk_add_f32 v[176:177], v[178:179], v[76:77]
	v_pk_add_f32 v[76:77], v[180:181], v[198:199]
	v_pk_add_f32 v[178:179], v[182:183], v[78:79]
	v_pk_add_f32 v[78:79], v[184:185], v[200:201]
	v_mul_f32_e32 v180, v161, v161
	v_mul_f32_e32 v181, v163, v163
	v_mul_f32_e32 v182, v63, v63
	v_mul_f32_e32 v183, v175, v175
	v_cvt_pk_bf16_f32 v60, v160, v161
	v_cvt_pk_bf16_f32 v61, v162, v163
	v_mul_f32_e32 v161, v77, v77
	v_mul_f32_e32 v163, v177, v177
	v_mul_f32_e32 v184, v79, v79
	v_mul_f32_e32 v185, v179, v179
	v_fmac_f32_e32 v180, v160, v160
	v_fmac_f32_e32 v181, v162, v162
	v_fmac_f32_e32 v182, v62, v62
	v_fmac_f32_e32 v183, v174, v174
	v_fmac_f32_e32 v161, v76, v76
	v_fmac_f32_e32 v163, v176, v176
	v_fmac_f32_e32 v184, v78, v78
	v_fmac_f32_e32 v185, v178, v178
	v_add_f32_e32 v160, v180, v181
	v_add_f32_e32 v162, v182, v183
	v_add_f32_e32 v161, v161, v163
	v_add_f32_e32 v163, v184, v185
	v_add_f32_e32 v160, v160, v162
	v_add_f32_e32 v161, v161, v163
	v_add_f32_e32 v160, v160, v161
	ds_bpermute_b32 v161, v190, v160
	v_cvt_pk_bf16_f32 v62, v62, v63
	v_cvt_pk_bf16_f32 v63, v174, v175
	global_store_dwordx4 v[192:193], v[60:63], off
	v_cvt_pk_bf16_f32 v76, v76, v77
	v_cvt_pk_bf16_f32 v77, v176, v177
	v_cvt_pk_bf16_f32 v78, v78, v79
	v_cvt_pk_bf16_f32 v79, v178, v179
	global_store_dwordx4 v[192:193], v[76:79], off offset:256
	s_waitcnt lgkmcnt(0)
	v_add_f32_e32 v60, v160, v161
	v_lshlrev_b32_e32 v160, 2, v202
	ds_bpermute_b32 v61, v160, v60
	s_and_saveexec_b64 s[44:45], s[36:37]
	s_cbranch_execz .LBB0_824
	v_lshlrev_b64 v[62:63], 7, v[38:39]
	v_lshl_add_u64 v[62:63], s[22:23], 0, v[62:63]
	v_lshl_add_u64 v[62:63], s[42:43], 2, v[62:63]
	s_lshl_b32 s46, s62, 2
	s_mov_b32 s47, s31
	v_lshl_add_u64 v[62:63], v[62:63], 0, s[46:47]
	s_waitcnt lgkmcnt(0)
	v_add_f32_e32 v39, v60, v61
	global_store_dword v[62:63], v39, off

; #define PG8_ST16(rs, b0, p, v) __builtin_amdgcn_raw_buffer_store_b128(v, rs, (int)((const char*)(p) - (const char*)(b0)), 0, 16)
; __device__ __forceinline__ unsigned cvt_pk_bf16(float lo, float hi) { unsigned r; asm volatile("v_cvt_pk_bf16_f32 %0, %1, %2" : "=v"(r) : "v"(lo), "v"(hi)); return r; }
;     __device__ __forceinline__ void operator()(const f32x4 (&acc)[2][2][4][2], const Unit& u, int wr, int wc, int fr, int fq) const {
;     ...
;             for (int m = 0; m < 4; ++m) { const size_t off = (size_t)(row0 + ai * HALF + m * 16) * ldc + col0;
; #pragma unroll
;                 for (int bj = 0; bj < 2; ++bj) {
;                     if (BASE_F32) { b0[m][bj] = *(const f32x4*)((const float*)base + off + bj * HALF); b1[m][bj] = *(const f32x4*)((const float*)base + off + bj * HALF + 4); }
;                     else { const u32x4 q = *(const u32x4*)((const bf16_t*)base + off + bj * HALF);
;                         b0[m][bj] = (f32x4){__uint_as_float(q.x << 16), __uint_as_float(q.x & 0xffff0000u), __uint_as_float(q.y << 16), __uint_as_float(q.y & 0xffff0000u)};
;                         b1[m][bj] = (f32x4){__uint_as_float(q.z << 16), __uint_as_float(q.z & 0xffff0000u), __uint_as_float(q.w << 16), __uint_as_float(q.w & 0xffff0000u)}; } } }
;             asm volatile("" ::: "memory");
; #pragma unroll
;             for (int m = 0; m < 4; ++m) { const size_t off = (size_t)(row0 + ai * HALF + m * 16) * ldc + col0; float ssq = 0.f;
; #pragma unroll
;                 for (int bj = 0; bj < 2; ++bj) {
;                     const f32x4 o0 = b0[m][bj] + acc[ai][bj][m][0] * sc, o1 = b1[m][bj] + acc[ai][bj][m][1] * sc;
;                     ssq += ((o0[0] * o0[0] + o0[1] * o0[1]) + (o0[2] * o0[2] + o0[3] * o0[3])) + ((o1[0] * o1[0] + o1[1] * o1[1]) + (o1[2] * o1[2] + o1[3] * o1[3]));
;                     u32x4 w; w.x = cvt_pk_bf16(o0[0], o0[1]); w.y = cvt_pk_bf16(o0[2], o0[3]); w.z = cvt_pk_bf16(o1[0], o1[1]); w.w = cvt_pk_bf16(o1[2], o1[3]);
;                     PG8_ST16(rs_, out, out + off + bj * HALF, w); }
;                 ssq += __shfl_xor(ssq, 16); ssq += __shfl_xor(ssq, 32);
;                 if (fq == 0) rowss[(size_t)(row0 + ai * HALF + m * 16) * 32 + 4 * u.pn + wc] = ssq; }
.LBB0_830:
	s_or_b64 exec, exec, s[44:45]
	v_add_u32_e32 v54, 0x80, v38
	v_ashrrev_i32_e32 v55, 31, v54
	v_lshlrev_b64 v[112:113], 12, v[54:55]
	v_lshl_add_u64 v[8:9], v[40:41], 0, v[112:113]
	s_waitcnt lgkmcnt(0)
	s_waitcnt vmcnt(8)
	v_add_u32_e32 v52, 0x90, v38
	v_ashrrev_i32_e32 v53, 31, v52
	v_add_u32_e32 v42, 0xa0, v38
	v_ashrrev_i32_e32 v43, 31, v42
	v_add_u32_e32 v38, 0xb0, v38
	v_ashrrev_i32_e32 v39, 31, v38
	v_mov_b32_e32 v24, v226
	v_mov_b32_e32 v25, v227
	v_mov_b32_e32 v26, v228
	v_mov_b32_e32 v27, v229
	v_mov_b32_e32 v20, v230
	v_mov_b32_e32 v21, v231
	v_mov_b32_e32 v22, v232
	v_mov_b32_e32 v23, v233
	v_mov_b32_e32 v16, v234
	v_mov_b32_e32 v17, v235
	v_mov_b32_e32 v18, v236
	v_mov_b32_e32 v19, v237
	v_mov_b32_e32 v12, v238
	v_mov_b32_e32 v13, v239
	v_mov_b32_e32 v14, v240
	v_mov_b32_e32 v15, v241
	v_mov_b32_e32 v8, v242
	v_mov_b32_e32 v9, v243
	v_mov_b32_e32 v10, v244
	v_mov_b32_e32 v11, v245
	v_mov_b32_e32 v4, v246
	v_mov_b32_e32 v5, v247
	v_mov_b32_e32 v6, v248
	v_mov_b32_e32 v7, v249
	v_lshlrev_b32_e32 v116, 16, v222
	v_and_b32_e32 v117, 0xffff0000, v222
	v_lshlrev_b32_e32 v120, 16, v223
	v_and_b32_e32 v121, 0xffff0000, v223
	v_lshlrev_b32_e32 v114, 16, v224
	v_and_b32_e32 v115, 0xffff0000, v224
	v_lshlrev_b32_e32 v118, 16, v225
	v_and_b32_e32 v119, 0xffff0000, v225
	v_pk_add_f32 v[108:109], v[108:109], v[116:117]
	v_lshlrev_b32_e32 v62, 16, v218
	v_and_b32_e32 v63, 0xffff0000, v218
	v_lshlrev_b32_e32 v78, 16, v219
	v_and_b32_e32 v79, 0xffff0000, v219
	v_lshlrev_b32_e32 v60, 16, v220
	v_and_b32_e32 v61, 0xffff0000, v220
	v_lshlrev_b32_e32 v76, 16, v221
	v_and_b32_e32 v77, 0xffff0000, v221
	v_pk_add_f32 v[40:41], v[110:111], v[120:121]
	v_pk_add_f32 v[78:79], v[102:103], v[78:79]
	v_pk_add_f32 v[62:63], v[100:101], v[62:63]
	v_pk_add_f32 v[110:111], v[106:107], v[118:119]
	v_pk_add_f32 v[106:107], v[104:105], v[114:115]
	v_mul_f32_e32 v104, v109, v109
	v_mul_f32_e32 v105, v41, v41
	v_pk_add_f32 v[96:97], v[96:97], v[60:61]
	v_mul_f32_e32 v60, v63, v63
	v_mul_f32_e32 v61, v79, v79
	v_fmac_f32_e32 v104, v108, v108
	v_fmac_f32_e32 v105, v40, v40
	v_pk_add_f32 v[76:77], v[98:99], v[76:77]
	v_fmac_f32_e32 v60, v62, v62
	v_fmac_f32_e32 v61, v78, v78
	v_add_f32_e32 v104, v104, v105
	v_mul_f32_e32 v105, v107, v107
	v_mul_f32_e32 v114, v111, v111
	v_add_f32_e32 v60, v60, v61
	v_mul_f32_e32 v61, v97, v97
	v_mul_f32_e32 v98, v77, v77
	v_fmac_f32_e32 v105, v106, v106
	v_fmac_f32_e32 v114, v110, v110
	v_fmac_f32_e32 v61, v96, v96
	v_fmac_f32_e32 v98, v76, v76
	v_add_f32_e32 v105, v105, v114
	v_add_f32_e32 v61, v61, v98
	v_add_f32_e32 v114, v104, v105
	v_cvt_pk_bf16_f32 v104, v108, v109
	v_cvt_pk_bf16_f32 v105, v40, v41
	v_lshl_add_u64 v[40:41], s[20:21], 0, v[112:113]
	v_add_f32_e32 v60, v60, v61
	v_lshl_add_u64 v[40:41], v[36:37], 1, v[40:41]
	v_add_f32_e32 v98, v114, v60
	v_cvt_pk_bf16_f32 v106, v106, v107
	v_cvt_pk_bf16_f32 v107, v110, v111
	global_store_dwordx4 v[40:41], v[104:107], off
	v_cvt_pk_bf16_f32 v60, v62, v63
	v_cvt_pk_bf16_f32 v61, v78, v79
	v_cvt_pk_bf16_f32 v62, v96, v97
	v_cvt_pk_bf16_f32 v63, v76, v77
	global_store_dwordx4 v[40:41], v[60:63], off offset:256
	ds_bpermute_b32 v40, v190, v98
	s_waitcnt lgkmcnt(0)
	v_add_f32_e32 v40, v98, v40
	ds_bpermute_b32 v41, v160, v40
	s_and_saveexec_b64 s[44:45], s[36:37]
	s_cbranch_execz .LBB0_832
	v_lshlrev_b64 v[54:55], 7, v[54:55]
	v_lshl_add_u64 v[54:55], s[22:23], 0, v[54:55]
	v_lshl_add_u64 v[54:55], s[42:43], 2, v[54:55]
	s_lshl_b32 s46, s62, 2
	s_mov_b32 s47, s31
	v_lshl_add_u64 v[54:55], v[54:55], 0, s[46:47]
	s_waitcnt lgkmcnt(0)
	v_add_f32_e32 v40, v40, v41
	global_store_dword v[54:55], v40, off
